# P14 rewrite + P16 SwiGLU-fp8 epilogue hand-written with packed f32 VALU (fewer instructions)
# speedup vs baseline: 1.0032x; 1.0032x over previous
; #define NEXT_ROW(roff, m, LD) do { roff += (size_t)((m) == 3 ? 80 : 16) * (LD); asm volatile("" : "+v"(roff) :: "memory"); } while (0)
;     __device__ __forceinline__ void operator()(Acc& acc, const Unit& u, int wr, int wc, int fr, int fq, LAS unsigned char* le, int wid, int lane, int& cpm) const {
;     ...
;         size_t roff = (size_t)(row0 + wr * 64 + fr) * DFF + u.pn * 128 + wc * 32 + fq * 8;
; #pragma unroll
;         for (int ai = 0; ai < 2; ++ai)
; #pragma unroll
;             for (int m = 0; m < 4; ++m) { const int rt = ai * 128 + wr * 64 + m * 16 + fr; const float rs = S[rt];
;                 const float rl = rs * -1.4426950408889634f, kk = rs * rs * H_SCALE; f32x4 ha, hb;
; #pragma unroll
;                 for (int j = 0; j < 4; ++j) { const float g0 = acc[ai][0][m][0][j], g1 = acc[ai][0][m][1][j];
;                     ha[j] = (g0 * acc[ai][1][m][0][j]) * kk * __builtin_amdgcn_rcpf(1.0f + __builtin_amdgcn_exp2f(g0 * rl));
;                     hb[j] = (g1 * acc[ai][1][m][1][j]) * kk * __builtin_amdgcn_rcpf(1.0f + __builtin_amdgcn_exp2f(g1 * rl)); }
;                 u32x2 w; w.x = pk4_fp8(ha[0], ha[1], ha[2], ha[3]); w.y = pk4_fp8(hb[0], hb[1], hb[2], hb[3]);
;                 ST_NT((u32x2*)(out + roff), w);
;                 NEXT_ROW(roff, m, DFF); }
.LBB0_2098:
	ds_read_b32 v204, v198
	ds_read_b32 v205, v198 offset:64
	ds_read_b32 v206, v198 offset:128
	ds_read_b32 v207, v198 offset:192
	ds_read_b32 v208, v198 offset:512
	ds_read_b32 v209, v198 offset:576
	ds_read_b32 v210, v198 offset:640
	ds_read_b32 v211, v198 offset:704
	s_lshl_b32 s36, s34, 7
	s_ashr_i32 s37, s36, 31
	v_add_u32_e32 v4, s11, v194
	v_lshl_add_u64 v[0:1], v[172:173], 0, s[36:37]
	v_mad_i64_i32 v[0:1], s[36:37], v4, s65, v[0:1]
	v_lshl_add_u64 v[0:1], s[14:15], 0, v[0:1]
	s_waitcnt lgkmcnt(0)
	v_mul_f32_e32 v212, 0xbfb8aa3b, v204
	v_mul_f32_e32 v214, v204, v204
	v_pk_mul_f32 v[224:225], v[156:157], v[148:149]
	v_pk_mul_f32 v[226:227], v[158:159], v[150:151]
	v_pk_mul_f32 v[228:229], v[152:153], v[144:145]
	v_pk_mul_f32 v[230:231], v[154:155], v[146:147]
	v_mul_f32_e32 v214, 0x41000000, v214
	v_pk_mul_f32 v[216:217], v[156:157], v[212:213] op_sel_hi:[1,0]
	v_pk_mul_f32 v[218:219], v[158:159], v[212:213] op_sel_hi:[1,0]
	v_pk_mul_f32 v[220:221], v[152:153], v[212:213] op_sel_hi:[1,0]
	v_pk_mul_f32 v[222:223], v[154:155], v[212:213] op_sel_hi:[1,0]
	v_rcp_f32_e32 v214, v214
	v_exp_f32_e32 v216, v216
	v_exp_f32_e32 v217, v217
	v_exp_f32_e32 v218, v218
	v_exp_f32_e32 v219, v219
	v_exp_f32_e32 v220, v220
	v_exp_f32_e32 v221, v221
	v_exp_f32_e32 v222, v222
	v_exp_f32_e32 v223, v223
	v_pk_fma_f32 v[216:217], v[216:217], v[214:215], v[214:215] op_sel_hi:[1,0,0]
	v_pk_fma_f32 v[218:219], v[218:219], v[214:215], v[214:215] op_sel_hi:[1,0,0]
	v_pk_fma_f32 v[220:221], v[220:221], v[214:215], v[214:215] op_sel_hi:[1,0,0]
	v_pk_fma_f32 v[222:223], v[222:223], v[214:215], v[214:215] op_sel_hi:[1,0,0]
	v_rcp_f32_e32 v216, v216
	v_rcp_f32_e32 v217, v217
	v_rcp_f32_e32 v218, v218
	v_rcp_f32_e32 v219, v219
	v_rcp_f32_e32 v220, v220
	v_rcp_f32_e32 v221, v221
	v_rcp_f32_e32 v222, v222
	v_rcp_f32_e32 v223, v223
	v_pk_mul_f32 v[224:225], v[224:225], v[216:217]
	v_pk_mul_f32 v[226:227], v[226:227], v[218:219]
	v_pk_mul_f32 v[228:229], v[228:229], v[220:221]
	v_pk_mul_f32 v[230:231], v[230:231], v[222:223]
	v_med3_f32 v224, v224, s66, v202
	v_med3_f32 v225, v225, s66, v202
	v_med3_f32 v226, v226, s66, v202
	v_med3_f32 v227, v227, s66, v202
	v_med3_f32 v228, v228, s66, v202
	v_med3_f32 v229, v229, s66, v202
	v_med3_f32 v230, v230, s66, v202
	v_med3_f32 v231, v231, s66, v202
	v_cvt_pk_fp8_f32 v2, v224, v225
	v_cvt_pk_fp8_f32 v3, v228, v229
	v_cvt_pk_fp8_f32 v2, v226, v227 op_sel:[0,0,1]
	v_cvt_pk_fp8_f32 v3, v230, v231 op_sel:[0,0,1]
	s_nop 0
	global_store_dwordx2 v[0:1], v[2:3], off
	v_lshl_add_u64 v[0:1], v[0:1], 0, s[24:25]
	v_mul_f32_e32 v212, 0xbfb8aa3b, v205
	v_mul_f32_e32 v214, v205, v205
	v_pk_mul_f32 v[224:225], v[140:141], v[132:133]
	v_pk_mul_f32 v[226:227], v[142:143], v[134:135]
	v_pk_mul_f32 v[228:229], v[136:137], v[128:129]
	v_pk_mul_f32 v[230:231], v[138:139], v[130:131]
	v_mul_f32_e32 v214, 0x41000000, v214
	v_pk_mul_f32 v[216:217], v[140:141], v[212:213] op_sel_hi:[1,0]
	v_pk_mul_f32 v[218:219], v[142:143], v[212:213] op_sel_hi:[1,0]
	v_pk_mul_f32 v[220:221], v[136:137], v[212:213] op_sel_hi:[1,0]
	v_pk_mul_f32 v[222:223], v[138:139], v[212:213] op_sel_hi:[1,0]
	v_rcp_f32_e32 v214, v214
	v_exp_f32_e32 v216, v216
	v_exp_f32_e32 v217, v217
	v_exp_f32_e32 v218, v218
	v_exp_f32_e32 v219, v219
	v_exp_f32_e32 v220, v220
	v_exp_f32_e32 v221, v221
	v_exp_f32_e32 v222, v222
	v_exp_f32_e32 v223, v223
	v_pk_fma_f32 v[216:217], v[216:217], v[214:215], v[214:215] op_sel_hi:[1,0,0]
	v_pk_fma_f32 v[218:219], v[218:219], v[214:215], v[214:215] op_sel_hi:[1,0,0]
	v_pk_fma_f32 v[220:221], v[220:221], v[214:215], v[214:215] op_sel_hi:[1,0,0]
	v_pk_fma_f32 v[222:223], v[222:223], v[214:215], v[214:215] op_sel_hi:[1,0,0]
	v_rcp_f32_e32 v216, v216
	v_rcp_f32_e32 v217, v217
	v_rcp_f32_e32 v218, v218
	v_rcp_f32_e32 v219, v219
	v_rcp_f32_e32 v220, v220
	v_rcp_f32_e32 v221, v221
	v_rcp_f32_e32 v222, v222
	v_rcp_f32_e32 v223, v223
	v_pk_mul_f32 v[224:225], v[224:225], v[216:217]
	v_pk_mul_f32 v[226:227], v[226:227], v[218:219]
	v_pk_mul_f32 v[228:229], v[228:229], v[220:221]
	v_pk_mul_f32 v[230:231], v[230:231], v[222:223]
	v_med3_f32 v224, v224, s66, v202
	v_med3_f32 v225, v225, s66, v202
	v_med3_f32 v226, v226, s66, v202
	v_med3_f32 v227, v227, s66, v202
	v_med3_f32 v228, v228, s66, v202
	v_med3_f32 v229, v229, s66, v202
	v_med3_f32 v230, v230, s66, v202
	v_med3_f32 v231, v231, s66, v202
	v_cvt_pk_fp8_f32 v2, v224, v225
	v_cvt_pk_fp8_f32 v3, v228, v229
	v_cvt_pk_fp8_f32 v2, v226, v227 op_sel:[0,0,1]
	v_cvt_pk_fp8_f32 v3, v230, v231 op_sel:[0,0,1]
	s_nop 0
	global_store_dwordx2 v[0:1], v[2:3], off
	v_lshl_add_u64 v[0:1], v[0:1], 0, s[24:25]
	v_mul_f32_e32 v212, 0xbfb8aa3b, v206
	v_mul_f32_e32 v214, v206, v206
	v_pk_mul_f32 v[224:225], v[124:125], v[116:117]
	v_pk_mul_f32 v[226:227], v[126:127], v[118:119]
	v_pk_mul_f32 v[228:229], v[120:121], v[112:113]
	v_pk_mul_f32 v[230:231], v[122:123], v[114:115]
	v_mul_f32_e32 v214, 0x41000000, v214
	v_pk_mul_f32 v[216:217], v[124:125], v[212:213] op_sel_hi:[1,0]
	v_pk_mul_f32 v[218:219], v[126:127], v[212:213] op_sel_hi:[1,0]
	v_pk_mul_f32 v[220:221], v[120:121], v[212:213] op_sel_hi:[1,0]
	v_pk_mul_f32 v[222:223], v[122:123], v[212:213] op_sel_hi:[1,0]
	v_rcp_f32_e32 v214, v214
	v_exp_f32_e32 v216, v216
	v_exp_f32_e32 v217, v217
	v_exp_f32_e32 v218, v218
	v_exp_f32_e32 v219, v219
	v_exp_f32_e32 v220, v220
	v_exp_f32_e32 v221, v221
	v_exp_f32_e32 v222, v222
	v_exp_f32_e32 v223, v223
	v_pk_fma_f32 v[216:217], v[216:217], v[214:215], v[214:215] op_sel_hi:[1,0,0]
	v_pk_fma_f32 v[218:219], v[218:219], v[214:215], v[214:215] op_sel_hi:[1,0,0]
	v_pk_fma_f32 v[220:221], v[220:221], v[214:215], v[214:215] op_sel_hi:[1,0,0]
; #define NEXT_ROW(roff, m, LD) do { roff += (size_t)((m) == 3 ? 80 : 16) * (LD); asm volatile("" : "+v"(roff) :: "memory"); } while (0)
;     __device__ __forceinline__ void operator()(Acc& acc, const Unit& u, int wr, int wc, int fr, int fq, LAS unsigned char* le, int wid, int lane, int& cpm) const {
;     ...
;             for (int m = 0; m < 4; ++m) { const int rt = ai * 128 + wr * 64 + m * 16 + fr; const float rs = S[rt];
;                 const float rl = rs * -1.4426950408889634f, kk = rs * rs * H_SCALE; f32x4 ha, hb;
; #pragma unroll
;                 for (int j = 0; j < 4; ++j) { const float g0 = acc[ai][0][m][0][j], g1 = acc[ai][0][m][1][j];
;                     ha[j] = (g0 * acc[ai][1][m][0][j]) * kk * __builtin_amdgcn_rcpf(1.0f + __builtin_amdgcn_exp2f(g0 * rl));
;                     hb[j] = (g1 * acc[ai][1][m][1][j]) * kk * __builtin_amdgcn_rcpf(1.0f + __builtin_amdgcn_exp2f(g1 * rl)); }
;                 u32x2 w; w.x = pk4_fp8(ha[0], ha[1], ha[2], ha[3]); w.y = pk4_fp8(hb[0], hb[1], hb[2], hb[3]);
;                 ST_NT((u32x2*)(out + roff), w);
;                 NEXT_ROW(roff, m, DFF); }
	v_pk_fma_f32 v[222:223], v[222:223], v[214:215], v[214:215] op_sel_hi:[1,0,0]
	v_rcp_f32_e32 v216, v216
	v_rcp_f32_e32 v217, v217
	v_rcp_f32_e32 v218, v218
	v_rcp_f32_e32 v219, v219
	v_rcp_f32_e32 v220, v220
	v_rcp_f32_e32 v221, v221
	v_rcp_f32_e32 v222, v222
	v_rcp_f32_e32 v223, v223
	v_pk_mul_f32 v[224:225], v[224:225], v[216:217]
	v_pk_mul_f32 v[226:227], v[226:227], v[218:219]
	v_pk_mul_f32 v[228:229], v[228:229], v[220:221]
	v_pk_mul_f32 v[230:231], v[230:231], v[222:223]
	v_med3_f32 v224, v224, s66, v202
	v_med3_f32 v225, v225, s66, v202
	v_med3_f32 v226, v226, s66, v202
	v_med3_f32 v227, v227, s66, v202
	v_med3_f32 v228, v228, s66, v202
	v_med3_f32 v229, v229, s66, v202
	v_med3_f32 v230, v230, s66, v202
	v_med3_f32 v231, v231, s66, v202
	v_cvt_pk_fp8_f32 v2, v224, v225
	v_cvt_pk_fp8_f32 v3, v228, v229
	v_cvt_pk_fp8_f32 v2, v226, v227 op_sel:[0,0,1]
	v_cvt_pk_fp8_f32 v3, v230, v231 op_sel:[0,0,1]
	s_nop 0
	global_store_dwordx2 v[0:1], v[2:3], off
	v_lshl_add_u64 v[0:1], v[0:1], 0, s[24:25]
	v_mul_f32_e32 v212, 0xbfb8aa3b, v207
	v_mul_f32_e32 v214, v207, v207
	v_pk_mul_f32 v[224:225], v[108:109], v[100:101]
	v_pk_mul_f32 v[226:227], v[110:111], v[102:103]
	v_pk_mul_f32 v[228:229], v[104:105], v[96:97]
	v_pk_mul_f32 v[230:231], v[106:107], v[98:99]
	v_mul_f32_e32 v214, 0x41000000, v214
	v_pk_mul_f32 v[216:217], v[108:109], v[212:213] op_sel_hi:[1,0]
	v_pk_mul_f32 v[218:219], v[110:111], v[212:213] op_sel_hi:[1,0]
	v_pk_mul_f32 v[220:221], v[104:105], v[212:213] op_sel_hi:[1,0]
	v_pk_mul_f32 v[222:223], v[106:107], v[212:213] op_sel_hi:[1,0]
	v_rcp_f32_e32 v214, v214
	v_exp_f32_e32 v216, v216
	v_exp_f32_e32 v217, v217
	v_exp_f32_e32 v218, v218
	v_exp_f32_e32 v219, v219
	v_exp_f32_e32 v220, v220
	v_exp_f32_e32 v221, v221
	v_exp_f32_e32 v222, v222
	v_exp_f32_e32 v223, v223
	v_pk_fma_f32 v[216:217], v[216:217], v[214:215], v[214:215] op_sel_hi:[1,0,0]
	v_pk_fma_f32 v[218:219], v[218:219], v[214:215], v[214:215] op_sel_hi:[1,0,0]
	v_pk_fma_f32 v[220:221], v[220:221], v[214:215], v[214:215] op_sel_hi:[1,0,0]
	v_pk_fma_f32 v[222:223], v[222:223], v[214:215], v[214:215] op_sel_hi:[1,0,0]
	v_rcp_f32_e32 v216, v216
	v_rcp_f32_e32 v217, v217
	v_rcp_f32_e32 v218, v218
	v_rcp_f32_e32 v219, v219
	v_rcp_f32_e32 v220, v220
	v_rcp_f32_e32 v221, v221
	v_rcp_f32_e32 v222, v222
	v_rcp_f32_e32 v223, v223
	v_pk_mul_f32 v[224:225], v[224:225], v[216:217]
	v_pk_mul_f32 v[226:227], v[226:227], v[218:219]
	v_pk_mul_f32 v[228:229], v[228:229], v[220:221]
	v_pk_mul_f32 v[230:231], v[230:231], v[222:223]
	v_med3_f32 v224, v224, s66, v202
	v_med3_f32 v225, v225, s66, v202
	v_med3_f32 v226, v226, s66, v202
	v_med3_f32 v227, v227, s66, v202
	v_med3_f32 v228, v228, s66, v202
	v_med3_f32 v229, v229, s66, v202
	v_med3_f32 v230, v230, s66, v202
	v_med3_f32 v231, v231, s66, v202
	v_cvt_pk_fp8_f32 v2, v224, v225
	v_cvt_pk_fp8_f32 v3, v228, v229
	v_cvt_pk_fp8_f32 v2, v226, v227 op_sel:[0,0,1]
	v_cvt_pk_fp8_f32 v3, v230, v231 op_sel:[0,0,1]
	s_nop 0
	global_store_dwordx2 v[0:1], v[2:3], off
	v_lshl_add_u64 v[0:1], v[0:1], 0, s[26:27]
	v_mul_f32_e32 v212, 0xbfb8aa3b, v208
	v_mul_f32_e32 v214, v208, v208
	v_pk_mul_f32 v[224:225], v[92:93], v[84:85]
	v_pk_mul_f32 v[226:227], v[94:95], v[86:87]
	v_pk_mul_f32 v[228:229], v[88:89], v[80:81]
	v_pk_mul_f32 v[230:231], v[90:91], v[82:83]
	v_mul_f32_e32 v214, 0x41000000, v214
	v_pk_mul_f32 v[216:217], v[92:93], v[212:213] op_sel_hi:[1,0]
	v_pk_mul_f32 v[218:219], v[94:95], v[212:213] op_sel_hi:[1,0]
	v_pk_mul_f32 v[220:221], v[88:89], v[212:213] op_sel_hi:[1,0]
	v_pk_mul_f32 v[222:223], v[90:91], v[212:213] op_sel_hi:[1,0]
	v_rcp_f32_e32 v214, v214
	v_exp_f32_e32 v216, v216
	v_exp_f32_e32 v217, v217
	v_exp_f32_e32 v218, v218
	v_exp_f32_e32 v219, v219
	v_exp_f32_e32 v220, v220
	v_exp_f32_e32 v221, v221
	v_exp_f32_e32 v222, v222
	v_exp_f32_e32 v223, v223
	v_pk_fma_f32 v[216:217], v[216:217], v[214:215], v[214:215] op_sel_hi:[1,0,0]
	v_pk_fma_f32 v[218:219], v[218:219], v[214:215], v[214:215] op_sel_hi:[1,0,0]
	v_pk_fma_f32 v[220:221], v[220:221], v[214:215], v[214:215] op_sel_hi:[1,0,0]
	v_pk_fma_f32 v[222:223], v[222:223], v[214:215], v[214:215] op_sel_hi:[1,0,0]
	v_rcp_f32_e32 v216, v216
	v_rcp_f32_e32 v217, v217
	v_rcp_f32_e32 v218, v218
	v_rcp_f32_e32 v219, v219
	v_rcp_f32_e32 v220, v220
	v_rcp_f32_e32 v221, v221
	v_rcp_f32_e32 v222, v222
	v_rcp_f32_e32 v223, v223
	v_pk_mul_f32 v[224:225], v[224:225], v[216:217]
	v_pk_mul_f32 v[226:227], v[226:227], v[218:219]
	v_pk_mul_f32 v[228:229], v[228:229], v[220:221]
	v_pk_mul_f32 v[230:231], v[230:231], v[222:223]
	v_med3_f32 v224, v224, s66, v202
	v_med3_f32 v225, v225, s66, v202
	v_med3_f32 v226, v226, s66, v202
	v_med3_f32 v227, v227, s66, v202
	v_med3_f32 v228, v228, s66, v202
	v_med3_f32 v229, v229, s66, v202
	v_med3_f32 v230, v230, s66, v202
	v_med3_f32 v231, v231, s66, v202
	v_cvt_pk_fp8_f32 v2, v224, v225
	v_cvt_pk_fp8_f32 v3, v228, v229
	v_cvt_pk_fp8_f32 v2, v226, v227 op_sel:[0,0,1]
	v_cvt_pk_fp8_f32 v3, v230, v231 op_sel:[0,0,1]
	s_nop 0
	global_store_dwordx2 v[0:1], v[2:3], off
	v_lshl_add_u64 v[0:1], v[0:1], 0, s[24:25]
	v_mul_f32_e32 v212, 0xbfb8aa3b, v209
	v_mul_f32_e32 v214, v209, v209
	v_pk_mul_f32 v[224:225], v[76:77], v[68:69]
	v_pk_mul_f32 v[226:227], v[78:79], v[70:71]
	v_pk_mul_f32 v[228:229], v[72:73], v[64:65]
	v_pk_mul_f32 v[230:231], v[74:75], v[66:67]
	v_mul_f32_e32 v214, 0x41000000, v214
	v_pk_mul_f32 v[216:217], v[76:77], v[212:213] op_sel_hi:[1,0]
	v_pk_mul_f32 v[218:219], v[78:79], v[212:213] op_sel_hi:[1,0]
	v_pk_mul_f32 v[220:221], v[72:73], v[212:213] op_sel_hi:[1,0]
	v_pk_mul_f32 v[222:223], v[74:75], v[212:213] op_sel_hi:[1,0]
	v_rcp_f32_e32 v214, v214
; #define PG8_BAR __builtin_amdgcn_s_barrier()
; #define PG8_ACC_INIT(unit) do { if constexpr (Epi::ACC_INIT) { E.init(acc, unit, wr, wc, fr, fq); } else { \
;         _Pragma("unroll") for (int a = 0; a < 2; ++a) _Pragma("unroll") for (int b = 0; b < 2; ++b) _Pragma("unroll") for (int m = 0; m < 4; ++m) _Pragma("unroll") for (int n = 0; n < 2; ++n) acc[a][b][m][n] = (f32x4){0.f, 0.f, 0.f, 0.f}; } } while (0)
; #define NEXT_ROW(roff, m, LD) do { roff += (size_t)((m) == 3 ? 80 : 16) * (LD); asm volatile("" : "+v"(roff) :: "memory"); } while (0)
; template <class Epi, class Sched, class Prob>
; __device__ __forceinline__ void gemm_phase(LAS unsigned char* lds, LAS unsigned char* lds_epi, const Prob g, const Sched& S, const Epi& E, int wid) {
;     ...
;         if (!has_next) break;
;         PG8_ACC_INIT(nxt);
;         cur = nxt; cA = nA; cB = nB; ++ui;
;         if (wr == 1) PG8_BAR;
;     __device__ __forceinline__ void operator()(Acc& acc, const Unit& u, int wr, int wc, int fr, int fq, LAS unsigned char* le, int wid, int lane, int& cpm) const {
;     ...
;             for (int m = 0; m < 4; ++m) { const int rt = ai * 128 + wr * 64 + m * 16 + fr; const float rs = S[rt];
;                 const float rl = rs * -1.4426950408889634f, kk = rs * rs * H_SCALE; f32x4 ha, hb;
; #pragma unroll
;                 for (int j = 0; j < 4; ++j) { const float g0 = acc[ai][0][m][0][j], g1 = acc[ai][0][m][1][j];
;                     ha[j] = (g0 * acc[ai][1][m][0][j]) * kk * __builtin_amdgcn_rcpf(1.0f + __builtin_amdgcn_exp2f(g0 * rl));
;                     hb[j] = (g1 * acc[ai][1][m][1][j]) * kk * __builtin_amdgcn_rcpf(1.0f + __builtin_amdgcn_exp2f(g1 * rl)); }
;                 u32x2 w; w.x = pk4_fp8(ha[0], ha[1], ha[2], ha[3]); w.y = pk4_fp8(hb[0], hb[1], hb[2], hb[3]);
;                 ST_NT((u32x2*)(out + roff), w);
;                 NEXT_ROW(roff, m, DFF); }
	v_exp_f32_e32 v216, v216
	v_exp_f32_e32 v217, v217
	v_exp_f32_e32 v218, v218
	v_exp_f32_e32 v219, v219
	v_exp_f32_e32 v220, v220
	v_exp_f32_e32 v221, v221
	v_exp_f32_e32 v222, v222
	v_exp_f32_e32 v223, v223
	v_pk_fma_f32 v[216:217], v[216:217], v[214:215], v[214:215] op_sel_hi:[1,0,0]
	v_pk_fma_f32 v[218:219], v[218:219], v[214:215], v[214:215] op_sel_hi:[1,0,0]
	v_pk_fma_f32 v[220:221], v[220:221], v[214:215], v[214:215] op_sel_hi:[1,0,0]
	v_pk_fma_f32 v[222:223], v[222:223], v[214:215], v[214:215] op_sel_hi:[1,0,0]
	v_rcp_f32_e32 v216, v216
	v_rcp_f32_e32 v217, v217
	v_rcp_f32_e32 v218, v218
	v_rcp_f32_e32 v219, v219
	v_rcp_f32_e32 v220, v220
	v_rcp_f32_e32 v221, v221
	v_rcp_f32_e32 v222, v222
	v_rcp_f32_e32 v223, v223
	v_pk_mul_f32 v[224:225], v[224:225], v[216:217]
	v_pk_mul_f32 v[226:227], v[226:227], v[218:219]
	v_pk_mul_f32 v[228:229], v[228:229], v[220:221]
	v_pk_mul_f32 v[230:231], v[230:231], v[222:223]
	v_med3_f32 v224, v224, s66, v202
	v_med3_f32 v225, v225, s66, v202
	v_med3_f32 v226, v226, s66, v202
	v_med3_f32 v227, v227, s66, v202
	v_med3_f32 v228, v228, s66, v202
	v_med3_f32 v229, v229, s66, v202
	v_med3_f32 v230, v230, s66, v202
	v_med3_f32 v231, v231, s66, v202
	v_cvt_pk_fp8_f32 v2, v224, v225
	v_cvt_pk_fp8_f32 v3, v228, v229
	v_cvt_pk_fp8_f32 v2, v226, v227 op_sel:[0,0,1]
	v_cvt_pk_fp8_f32 v3, v230, v231 op_sel:[0,0,1]
	s_nop 0
	global_store_dwordx2 v[0:1], v[2:3], off
	v_lshl_add_u64 v[0:1], v[0:1], 0, s[24:25]
	v_mul_f32_e32 v212, 0xbfb8aa3b, v210
	v_mul_f32_e32 v214, v210, v210
	v_pk_mul_f32 v[224:225], v[60:61], v[52:53]
	v_pk_mul_f32 v[226:227], v[62:63], v[54:55]
	v_pk_mul_f32 v[228:229], v[56:57], v[48:49]
	v_pk_mul_f32 v[230:231], v[58:59], v[50:51]
	v_mul_f32_e32 v214, 0x41000000, v214
	v_pk_mul_f32 v[216:217], v[60:61], v[212:213] op_sel_hi:[1,0]
	v_pk_mul_f32 v[218:219], v[62:63], v[212:213] op_sel_hi:[1,0]
	v_pk_mul_f32 v[220:221], v[56:57], v[212:213] op_sel_hi:[1,0]
	v_pk_mul_f32 v[222:223], v[58:59], v[212:213] op_sel_hi:[1,0]
	v_rcp_f32_e32 v214, v214
	v_exp_f32_e32 v216, v216
	v_exp_f32_e32 v217, v217
	v_exp_f32_e32 v218, v218
	v_exp_f32_e32 v219, v219
	v_exp_f32_e32 v220, v220
	v_exp_f32_e32 v221, v221
	v_exp_f32_e32 v222, v222
	v_exp_f32_e32 v223, v223
	v_pk_fma_f32 v[216:217], v[216:217], v[214:215], v[214:215] op_sel_hi:[1,0,0]
	v_pk_fma_f32 v[218:219], v[218:219], v[214:215], v[214:215] op_sel_hi:[1,0,0]
	v_pk_fma_f32 v[220:221], v[220:221], v[214:215], v[214:215] op_sel_hi:[1,0,0]
	v_pk_fma_f32 v[222:223], v[222:223], v[214:215], v[214:215] op_sel_hi:[1,0,0]
	v_rcp_f32_e32 v216, v216
	v_rcp_f32_e32 v217, v217
	v_rcp_f32_e32 v218, v218
	v_rcp_f32_e32 v219, v219
	v_rcp_f32_e32 v220, v220
	v_rcp_f32_e32 v221, v221
	v_rcp_f32_e32 v222, v222
	v_rcp_f32_e32 v223, v223
	v_pk_mul_f32 v[224:225], v[224:225], v[216:217]
	v_pk_mul_f32 v[226:227], v[226:227], v[218:219]
	v_pk_mul_f32 v[228:229], v[228:229], v[220:221]
	v_pk_mul_f32 v[230:231], v[230:231], v[222:223]
	v_med3_f32 v224, v224, s66, v202
	v_med3_f32 v225, v225, s66, v202
	v_med3_f32 v226, v226, s66, v202
	v_med3_f32 v227, v227, s66, v202
	v_med3_f32 v228, v228, s66, v202
	v_med3_f32 v229, v229, s66, v202
	v_med3_f32 v230, v230, s66, v202
	v_med3_f32 v231, v231, s66, v202
	v_cvt_pk_fp8_f32 v2, v224, v225
	v_cvt_pk_fp8_f32 v3, v228, v229
	v_cvt_pk_fp8_f32 v2, v226, v227 op_sel:[0,0,1]
	v_cvt_pk_fp8_f32 v3, v230, v231 op_sel:[0,0,1]
	s_nop 0
	global_store_dwordx2 v[0:1], v[2:3], off
	v_lshl_add_u64 v[0:1], v[0:1], 0, s[24:25]
	v_mul_f32_e32 v212, 0xbfb8aa3b, v211
	v_mul_f32_e32 v214, v211, v211
	v_pk_mul_f32 v[224:225], v[44:45], v[36:37]
	v_pk_mul_f32 v[226:227], v[46:47], v[38:39]
	v_pk_mul_f32 v[228:229], v[40:41], v[32:33]
	v_pk_mul_f32 v[230:231], v[42:43], v[34:35]
	v_mul_f32_e32 v214, 0x41000000, v214
	v_pk_mul_f32 v[216:217], v[44:45], v[212:213] op_sel_hi:[1,0]
	v_pk_mul_f32 v[218:219], v[46:47], v[212:213] op_sel_hi:[1,0]
	v_pk_mul_f32 v[220:221], v[40:41], v[212:213] op_sel_hi:[1,0]
	v_pk_mul_f32 v[222:223], v[42:43], v[212:213] op_sel_hi:[1,0]
	v_rcp_f32_e32 v214, v214
	v_exp_f32_e32 v216, v216
	v_exp_f32_e32 v217, v217
	v_exp_f32_e32 v218, v218
	v_exp_f32_e32 v219, v219
	v_exp_f32_e32 v220, v220
	v_exp_f32_e32 v221, v221
	v_exp_f32_e32 v222, v222
	v_exp_f32_e32 v223, v223
	v_pk_fma_f32 v[216:217], v[216:217], v[214:215], v[214:215] op_sel_hi:[1,0,0]
	v_pk_fma_f32 v[218:219], v[218:219], v[214:215], v[214:215] op_sel_hi:[1,0,0]
	v_pk_fma_f32 v[220:221], v[220:221], v[214:215], v[214:215] op_sel_hi:[1,0,0]
	v_pk_fma_f32 v[222:223], v[222:223], v[214:215], v[214:215] op_sel_hi:[1,0,0]
	v_rcp_f32_e32 v216, v216
	v_rcp_f32_e32 v217, v217
	v_rcp_f32_e32 v218, v218
	v_rcp_f32_e32 v219, v219
	v_rcp_f32_e32 v220, v220
	v_rcp_f32_e32 v221, v221
	v_rcp_f32_e32 v222, v222
	v_rcp_f32_e32 v223, v223
	v_pk_mul_f32 v[224:225], v[224:225], v[216:217]
	v_pk_mul_f32 v[226:227], v[226:227], v[218:219]
	v_pk_mul_f32 v[228:229], v[228:229], v[220:221]
	v_pk_mul_f32 v[230:231], v[230:231], v[222:223]
	v_med3_f32 v224, v224, s66, v202
	v_med3_f32 v225, v225, s66, v202
	v_med3_f32 v226, v226, s66, v202
	v_med3_f32 v227, v227, s66, v202
	v_med3_f32 v228, v228, s66, v202
	v_med3_f32 v229, v229, s66, v202
	v_med3_f32 v230, v230, s66, v202
	v_med3_f32 v231, v231, s66, v202
	v_cvt_pk_fp8_f32 v2, v224, v225
	v_cvt_pk_fp8_f32 v3, v228, v229
	v_cvt_pk_fp8_f32 v2, v226, v227 op_sel:[0,0,1]
	v_cvt_pk_fp8_f32 v3, v230, v231 op_sel:[0,0,1]
	s_nop 0
	global_store_dwordx2 v[0:1], v[2:3], off
	s_and_b64 vcc, exec, s[8:9]
	s_mov_b64 s[8:9], -1
	s_cbranch_vccnz .LBB0_2084
	s_and_b64 vcc, exec, s[4:5]
	s_cbranch_vccnz .LBB0_2083
	s_barrier
	s_branch .LBB0_2083
